# v28 + at_dil keeps the rel_bias LDS table at_mfma wrote (no reload + wait)
# baseline (speedup 1.0000x reference)
; __device__ __forceinline__ void at_dil(const Args& a, LAS unsigned char* lds, int layer) {
;     ...
;     { const int l64 = tid & 63;
;       float g2 = fabsf(a.in[I_QGD][layer * 64 + l64]), g3 = fabsf(a.in[I_KGD][layer * 64 + l64]);
;       float rbm = 0.f;
;       for (int i = l64; i < 32 * 6; i += 64) rbm = fmaxf(rbm, a.in[I_RELB][i]);
; #pragma unroll
;       for (int o2 = 1; o2 < 64; o2 <<= 1) { g2 = fmaxf(g2, __shfl_xor(g2, o2)); g3 = fmaxf(g3, __shfl_xor(g3, o2)); rbm = fmaxf(rbm, __shfl_xor(rbm, o2)); }
;       bdil = 8.f * g2 * g3 * LOG2E * 1.01f; bmax = fmaxf(rbm, 0.f) * LOG2E; }
;     const bool dil_fixed = (bdil + bmax) < 40.f;
;     const float m_dil = bdil + bmax;
;     const unsigned l0 = (unsigned)(uintptr_t)lds;
;     __syncthreads();
;     if (tid < 32 * 6) relb[tid] = a.in[I_RELB][tid] * LOG2E;
.LBB0_527:
	global_load_dword v8, v[2:3], off
	v_add_u32_e32 v7, 64, v7
	v_max_f32_e32 v6, v6, v6
	v_cmp_lt_u32_e32 vcc, s56, v7
	v_lshl_add_u64 v[2:3], v[2:3], 0, s[94:95]
	s_or_b64 s[4:5], vcc, s[4:5]
	s_waitcnt vmcnt(0)
	v_max_f32_e32 v8, v8, v8
	v_max_f32_e32 v6, v6, v8
	s_andn2_b64 exec, exec, s[4:5]
	s_cbranch_execnz .LBB0_527
	s_or_b64 exec, exec, s[4:5]
	v_and_b32_e32 v2, 0x7fffffff, v5
	ds_bpermute_b32 v2, v156, v2
	v_and_b32_e32 v3, 0x7fffffff, v4
	ds_bpermute_b32 v3, v156, v3
	ds_bpermute_b32 v7, v156, v6
	v_max_f32_e64 v5, |v5|, |v5|
	s_waitcnt lgkmcnt(2)
	v_max_f32_e32 v2, v2, v2
	v_max_f32_e32 v2, v5, v2
	s_waitcnt lgkmcnt(1)
	v_max_f32_e32 v3, v3, v3
	v_max_f32_e64 v4, |v4|, |v4|
	v_max_f32_e32 v3, v4, v3
	ds_bpermute_b32 v4, v158, v2
	s_waitcnt lgkmcnt(1)
	v_max_f32_e32 v5, v7, v7
	v_max_f32_e32 v6, v6, v6
	ds_bpermute_b32 v7, v158, v3
	v_max_f32_e32 v5, v6, v5
	ds_bpermute_b32 v6, v158, v5
	s_waitcnt lgkmcnt(2)
	v_max_f32_e32 v4, v4, v4
	v_max_f32_e32 v2, v2, v4
	s_waitcnt lgkmcnt(1)
	v_max_f32_e32 v4, v7, v7
	ds_bpermute_b32 v7, v159, v2
	v_max_f32_e32 v3, v3, v4
	s_waitcnt lgkmcnt(1)
	v_max_f32_e32 v4, v6, v6
	ds_bpermute_b32 v6, v159, v3
	v_max_f32_e32 v4, v5, v4
	s_waitcnt lgkmcnt(1)
	v_max_f32_e32 v5, v7, v7
	ds_bpermute_b32 v7, v159, v4
	v_max_f32_e32 v2, v2, v5
	s_waitcnt lgkmcnt(1)
	v_max_f32_e32 v5, v6, v6
	ds_bpermute_b32 v6, v160, v2
	v_max_f32_e32 v3, v3, v5
	s_waitcnt lgkmcnt(1)
	v_max_f32_e32 v5, v7, v7
	ds_bpermute_b32 v7, v160, v3
	v_max_f32_e32 v4, v4, v5
	s_waitcnt lgkmcnt(1)
	v_max_f32_e32 v5, v6, v6
	ds_bpermute_b32 v6, v160, v4
	v_max_f32_e32 v2, v2, v5
	s_waitcnt lgkmcnt(1)
	v_max_f32_e32 v5, v7, v7
	v_max_f32_e32 v3, v3, v5
	ds_bpermute_b32 v5, v250, v2
	s_waitcnt lgkmcnt(1)
	v_max_f32_e32 v6, v6, v6
	ds_bpermute_b32 v7, v250, v3
	v_max_f32_e32 v6, v4, v6
	ds_bpermute_b32 v8, v250, v6
	s_waitcnt lgkmcnt(2)
	v_max_f32_e32 v4, v5, v5
	v_max_f32_e32 v2, v2, v4
	s_waitcnt lgkmcnt(1)
	v_max_f32_e32 v4, v7, v7
	v_max_f32_e32 v4, v3, v4
	s_waitcnt lgkmcnt(0)
	v_max_f32_e32 v3, v8, v8
	v_max_f32_e32 v5, v6, v3
	ds_bpermute_b32 v3, v251, v2
	ds_bpermute_b32 v6, v251, v4
	ds_bpermute_b32 v7, v251, v5
	s_movk_i32 s2, 0
	v_cmp_gt_i32_e32 vcc, s2, v18
	s_waitcnt lgkmcnt(0)
	s_barrier
	s_and_saveexec_b64 s[4:5], vcc
	s_cbranch_execz .LBB0_530
	v_readlane_b32 s8, v252, 41
	v_ashrrev_i32_e32 v19, 31, v18
	v_readlane_b32 s9, v252, 42
	v_readlane_b32 s10, v252, 43
	v_readlane_b32 s11, v252, 44
	v_lshl_add_u64 v[8:9], v[18:19], 2, s[8:9]
	global_load_dword v8, v[8:9], off
	v_lshl_add_u32 v9, v18, 2, 0
	v_add_u32_e32 v9, 0x21f00, v9
	v_readlane_b32 s12, v252, 45
	v_readlane_b32 s13, v252, 46
	v_readlane_b32 s14, v252, 47
	v_readlane_b32 s15, v252, 48
	s_waitcnt vmcnt(0)
	v_mul_f32_e32 v8, 0x3fb8aa3b, v8
	ds_write_b32 v9, v8
